# moe_build_tiles: expert-of-tile table filled in parallel (one thread per tile counts prefix entries) instead of 32 serialized LDS-dependent blocks; m1
# speedup vs baseline: 1.0115x; 1.0012x over previous
; #define LAS __attribute__((address_space(3)))
; __device__ __forceinline__ int moe_build_tiles(const Args& a, LAS unsigned char* lds, int tid) {
;     unsigned* ctl = (unsigned*)(a.ws + WS_CTL);
;     LAS int* tp = (LAS int*)(lds + MISC_OFF + 1024); LAS int* te = (LAS int*)(lds + TE_OFF); LAS unsigned* cn = (LAS unsigned*)(lds + CNT_OFF);
;     if (tid < NEXP) cn[tid] = __hip_atomic_load(ctl + CW_CNT + 64 * tid, __ATOMIC_RELAXED, __HIP_MEMORY_SCOPE_AGENT);
;     __syncthreads();
;     if (tid == 0) { int s = 0; for (int e = 0; e < NEXP; ++e) { tp[e] = s; s += (int)((cn[e] + 255u) >> 8); } tp[NEXP] = s; }
;     __syncthreads();
;     for (int e = 0; e < NEXP; ++e) { const int lo = tp[e], hi = tp[e + 1]; for (int t = lo + tid; t < hi; t += 512) te[t] = e; }
;     __syncthreads();
;     return tp[NEXP];
; __global__ void __launch_bounds__(NWAVES * 64, 2) fwd(Args args) {
;     ...
;         const int ntiles = __builtin_amdgcn_readfirstlane(moe_build_tiles(args, lds, tid));
;         pg8::MoeOrder<true> S; S.init((const bf16*)(ws + WS_U2), (const bf16*)(ws + WS_WGU), ntiles, 4096, lds, ctl + CW_QUEUE + 64 * (bx & 7), bx & 7);
;         {
;             const LAS int* tp = (const LAS int*)(lds + MISC_OFF + 1024); const LAS unsigned* cn = (const LAS unsigned*)(lds + CNT_OFF); const LAS int* te = (const LAS int*)(lds + TE_OFF);
;             LAS unsigned short* gidx = (LAS unsigned short*)(lds + IDX_OFF); const int* elist = (const int*)(ws + WS_ELIST);
;             const int total = (ntiles - S.mlo < IDX_TILES ? ntiles - S.mlo : IDX_TILES) * 256;
; #pragma unroll 4
;             for (int q = tid; q < total; q += 512) { const int T = S.mlo + (q >> 8), e = te[T], rank = (T - tp[e]) * 256 + (q & 255); gidx[q] = (unsigned short)elist[(size_t)e * NTOK + (rank < (int)cn[e] ? rank : 0)]; }
.LBB0_1009:
	s_or_b64 exec, exec, s[2:3]
	s_add_i32 s12, 0, 0x20400
	v_mov_b32_e32 v1, s12
	s_waitcnt lgkmcnt(0)
	s_barrier
	s_waitcnt vmcnt(23)
	v_mov_b32_e32 v247, -1
	ds_read_b128 v[248:251], v1
	s_waitcnt lgkmcnt(0)
	v_cmp_le_i32_e32 vcc, v248, v0
	s_nop 1
	v_addc_co_u32_e32 v247, vcc, 0, v247, vcc
	v_cmp_le_i32_e32 vcc, v249, v0
	s_nop 1
	v_addc_co_u32_e32 v247, vcc, 0, v247, vcc
	v_cmp_le_i32_e32 vcc, v250, v0
	s_nop 1
	v_addc_co_u32_e32 v247, vcc, 0, v247, vcc
	v_cmp_le_i32_e32 vcc, v251, v0
	s_nop 1
	v_addc_co_u32_e32 v247, vcc, 0, v247, vcc
	ds_read_b128 v[248:251], v1 offset:16
	s_waitcnt lgkmcnt(0)
	v_cmp_le_i32_e32 vcc, v248, v0
	s_nop 1
	v_addc_co_u32_e32 v247, vcc, 0, v247, vcc
	v_cmp_le_i32_e32 vcc, v249, v0
	s_nop 1
	v_addc_co_u32_e32 v247, vcc, 0, v247, vcc
	v_cmp_le_i32_e32 vcc, v250, v0
	s_nop 1
	v_addc_co_u32_e32 v247, vcc, 0, v247, vcc
	v_cmp_le_i32_e32 vcc, v251, v0
	s_nop 1
	v_addc_co_u32_e32 v247, vcc, 0, v247, vcc
	ds_read_b128 v[248:251], v1 offset:32
	s_waitcnt lgkmcnt(0)
	v_cmp_le_i32_e32 vcc, v248, v0
	s_nop 1
	v_addc_co_u32_e32 v247, vcc, 0, v247, vcc
	v_cmp_le_i32_e32 vcc, v249, v0
	s_nop 1
	v_addc_co_u32_e32 v247, vcc, 0, v247, vcc
	v_cmp_le_i32_e32 vcc, v250, v0
	s_nop 1
	v_addc_co_u32_e32 v247, vcc, 0, v247, vcc
	v_cmp_le_i32_e32 vcc, v251, v0
	s_nop 1
	v_addc_co_u32_e32 v247, vcc, 0, v247, vcc
	ds_read_b128 v[248:251], v1 offset:48
	s_waitcnt lgkmcnt(0)
	v_cmp_le_i32_e32 vcc, v248, v0
	s_nop 1
	v_addc_co_u32_e32 v247, vcc, 0, v247, vcc
	v_cmp_le_i32_e32 vcc, v249, v0
	s_nop 1
	v_addc_co_u32_e32 v247, vcc, 0, v247, vcc
	v_cmp_le_i32_e32 vcc, v250, v0
	s_nop 1
	v_addc_co_u32_e32 v247, vcc, 0, v247, vcc
	v_cmp_le_i32_e32 vcc, v251, v0
	s_nop 1
	v_addc_co_u32_e32 v247, vcc, 0, v247, vcc
	ds_read_b128 v[248:251], v1 offset:64
	s_waitcnt lgkmcnt(0)
	v_cmp_le_i32_e32 vcc, v248, v0
	s_nop 1
	v_addc_co_u32_e32 v247, vcc, 0, v247, vcc
	v_cmp_le_i32_e32 vcc, v249, v0
	s_nop 1
	v_addc_co_u32_e32 v247, vcc, 0, v247, vcc
	v_cmp_le_i32_e32 vcc, v250, v0
	s_nop 1
	v_addc_co_u32_e32 v247, vcc, 0, v247, vcc
	v_cmp_le_i32_e32 vcc, v251, v0
	s_nop 1
	v_addc_co_u32_e32 v247, vcc, 0, v247, vcc
	ds_read_b128 v[248:251], v1 offset:80
	s_waitcnt lgkmcnt(0)
	v_cmp_le_i32_e32 vcc, v248, v0
	s_nop 1
	v_addc_co_u32_e32 v247, vcc, 0, v247, vcc
	v_cmp_le_i32_e32 vcc, v249, v0
	s_nop 1
	v_addc_co_u32_e32 v247, vcc, 0, v247, vcc
	v_cmp_le_i32_e32 vcc, v250, v0
	s_nop 1
	v_addc_co_u32_e32 v247, vcc, 0, v247, vcc
	v_cmp_le_i32_e32 vcc, v251, v0
	s_nop 1
	v_addc_co_u32_e32 v247, vcc, 0, v247, vcc
	ds_read_b128 v[248:251], v1 offset:96
	s_waitcnt lgkmcnt(0)
	v_cmp_le_i32_e32 vcc, v248, v0
	s_nop 1
	v_addc_co_u32_e32 v247, vcc, 0, v247, vcc
	v_cmp_le_i32_e32 vcc, v249, v0
	s_nop 1
	v_addc_co_u32_e32 v247, vcc, 0, v247, vcc
	v_cmp_le_i32_e32 vcc, v250, v0
	s_nop 1
	v_addc_co_u32_e32 v247, vcc, 0, v247, vcc
	v_cmp_le_i32_e32 vcc, v251, v0
	s_nop 1
	v_addc_co_u32_e32 v247, vcc, 0, v247, vcc
	ds_read_b128 v[248:251], v1 offset:112
	s_waitcnt lgkmcnt(0)
	v_cmp_le_i32_e32 vcc, v248, v0
	s_nop 1
	v_addc_co_u32_e32 v247, vcc, 0, v247, vcc
	v_cmp_le_i32_e32 vcc, v249, v0
	s_nop 1
	v_addc_co_u32_e32 v247, vcc, 0, v247, vcc
	v_cmp_le_i32_e32 vcc, v250, v0
	s_nop 1
	v_addc_co_u32_e32 v247, vcc, 0, v247, vcc
	v_cmp_le_i32_e32 vcc, v251, v0
	s_nop 1
	v_addc_co_u32_e32 v247, vcc, 0, v247, vcc
	ds_read_b32 v248, v1 offset:128
	s_waitcnt lgkmcnt(0)
	v_cmp_lt_i32_e32 vcc, v0, v248
	s_and_saveexec_b64 s[2:3], vcc
	v_lshlrev_b32_e32 v249, 2, v0
	v_add_u32_e32 v249, 0x21200, v249
	ds_write_b32 v249, v247
	s_or_b64 exec, exec, s[2:3]
	s_add_i32 s2, 0, 0x20480
	v_mov_b32_e32 v1, s2
	s_waitcnt lgkmcnt(0)
	s_barrier
	ds_read_b32 v1, v1
	v_readlane_b32 s2, v246, 12
	s_and_b32 s13, s2, 7
	s_waitcnt lgkmcnt(0)
	v_readfirstlane_b32 s27, v1
	s_lshl_b32 s52, s27, 1
	s_mul_i32 s53, s52, s13
	s_ashr_i32 s2, s53, 31
	s_lshr_b32 s2, s2, 25
	s_add_i32 s2, s53, s2
	s_ashr_i32 s17, s2, 7
	s_lshl_b32 s54, s17, 3
	s_sub_i32 s2, s27, s54
	s_min_i32 s2, s2, 48
	s_lshl_b32 s16, s2, 8
	v_cmp_gt_i32_e32 vcc, s16, v0
	s_and_saveexec_b64 s[2:3], vcc
	s_cbranch_execz .LBB0_1156
	v_not_b32_e32 v2, v0
	s_add_u32 s4, s92, 0x1a800000
	v_add_u32_e32 v3, s16, v2
	s_movk_i32 s6, 0x1ff
	s_addc_u32 s5, s93, 0
	v_and_b32_e32 v4, 0xff, v0
	v_cmp_lt_u32_e32 vcc, s6, v3
	s_mov_b64 s[8:9], -1
	v_mov_b32_e32 v1, v0
	s_and_saveexec_b64 s[6:7], vcc
	s_cbranch_execz .LBB0_1148
	v_lshrrev_b32_e32 v5, 9, v3
	v_add_u32_e32 v2, -1, v5
	v_or_b32_e32 v1, 0x200, v0
	v_lshrrev_b32_e32 v3, 1, v2
	s_mov_b32 s18, 0
	s_waitcnt vmcnt(22)
	v_add_u32_e32 v6, 1, v3
	v_cmp_lt_u32_e32 vcc, 5, v2
	v_mov_b32_e32 v9, 0
	v_mov_b64_e32 v[2:3], v[0:1]
	s_and_saveexec_b64 s[8:9], vcc
	s_cbranch_execz .LBB0_1142
	v_lshl_add_u32 v2, v0, 1, 0
	v_and_b32_e32 v7, -4, v6
	v_add_u32_e32 v8, 0x22000, v2
	s_mov_b64 s[10:11], 0
	s_add_i32 s19, 0, 0x21200
	s_add_i32 s20, 0, 0x20500
	v_mov_b64_e32 v[2:3], v[0:1]

; #define LAS __attribute__((address_space(3)))
;     __device__ __forceinline__ void prefetch(int i) const { if (threadIdx.x == 0) tick[(base + i) & 3] = (int)__hip_atomic_fetch_add(qctr, 1u, __ATOMIC_RELAXED, __HIP_MEMORY_SCOPE_AGENT); }
; __device__ __forceinline__ int moe_build_tiles(const Args& a, LAS unsigned char* lds, int tid) {
;     unsigned* ctl = (unsigned*)(a.ws + WS_CTL);
;     LAS int* tp = (LAS int*)(lds + MISC_OFF + 1024); LAS int* te = (LAS int*)(lds + TE_OFF); LAS unsigned* cn = (LAS unsigned*)(lds + CNT_OFF);
;     if (tid < NEXP) cn[tid] = __hip_atomic_load(ctl + CW_CNT + 64 * tid, __ATOMIC_RELAXED, __HIP_MEMORY_SCOPE_AGENT);
;     __syncthreads();
;     if (tid == 0) { int s = 0; for (int e = 0; e < NEXP; ++e) { tp[e] = s; s += (int)((cn[e] + 255u) >> 8); } tp[NEXP] = s; }
;     __syncthreads();
;     for (int e = 0; e < NEXP; ++e) { const int lo = tp[e], hi = tp[e + 1]; for (int t = lo + tid; t < hi; t += 512) te[t] = e; }
;     __syncthreads();
;     return tp[NEXP];
; __global__ void __launch_bounds__(NWAVES * 64, 2) fwd(Args args) {
;     ...
;         const int ntiles = __builtin_amdgcn_readfirstlane(moe_build_tiles(args, lds, tid));
;         pg8::MoeOrder<false> S; S.init((const bf16*)(ws + WS_ACT), (const bf16*)(ws + WS_WDN), ntiles, DM, lds, ctl + CW_QUEUE + 64 * (8 + (bx & 7)), bx & 7);
;         S.prefetch(0); S.prefetch(1); __syncthreads();
.LBB0_1308:
	s_or_b64 exec, exec, s[2:3]
	s_add_i32 s2, 0, 0x20400
	v_mov_b32_e32 v1, s2
	s_waitcnt lgkmcnt(0)
	s_barrier
	v_mov_b32_e32 v247, -1
	ds_read_b128 v[248:251], v1
	s_waitcnt lgkmcnt(0)
	v_cmp_le_i32_e32 vcc, v248, v0
	s_nop 1
	v_addc_co_u32_e32 v247, vcc, 0, v247, vcc
	v_cmp_le_i32_e32 vcc, v249, v0
	s_nop 1
	v_addc_co_u32_e32 v247, vcc, 0, v247, vcc
	v_cmp_le_i32_e32 vcc, v250, v0
	s_nop 1
	v_addc_co_u32_e32 v247, vcc, 0, v247, vcc
	v_cmp_le_i32_e32 vcc, v251, v0
	s_nop 1
	v_addc_co_u32_e32 v247, vcc, 0, v247, vcc
	ds_read_b128 v[248:251], v1 offset:16
	s_waitcnt lgkmcnt(0)
	v_cmp_le_i32_e32 vcc, v248, v0
	s_nop 1
	v_addc_co_u32_e32 v247, vcc, 0, v247, vcc
	v_cmp_le_i32_e32 vcc, v249, v0
	s_nop 1
	v_addc_co_u32_e32 v247, vcc, 0, v247, vcc
	v_cmp_le_i32_e32 vcc, v250, v0
	s_nop 1
	v_addc_co_u32_e32 v247, vcc, 0, v247, vcc
	v_cmp_le_i32_e32 vcc, v251, v0
	s_nop 1
	v_addc_co_u32_e32 v247, vcc, 0, v247, vcc
	ds_read_b128 v[248:251], v1 offset:32
	s_waitcnt lgkmcnt(0)
	v_cmp_le_i32_e32 vcc, v248, v0
	s_nop 1
	v_addc_co_u32_e32 v247, vcc, 0, v247, vcc
	v_cmp_le_i32_e32 vcc, v249, v0
	s_nop 1
	v_addc_co_u32_e32 v247, vcc, 0, v247, vcc
	v_cmp_le_i32_e32 vcc, v250, v0
	s_nop 1
	v_addc_co_u32_e32 v247, vcc, 0, v247, vcc
	v_cmp_le_i32_e32 vcc, v251, v0
	s_nop 1
	v_addc_co_u32_e32 v247, vcc, 0, v247, vcc
	ds_read_b128 v[248:251], v1 offset:48
	s_waitcnt lgkmcnt(0)
	v_cmp_le_i32_e32 vcc, v248, v0
	s_nop 1
	v_addc_co_u32_e32 v247, vcc, 0, v247, vcc
	v_cmp_le_i32_e32 vcc, v249, v0
	s_nop 1
	v_addc_co_u32_e32 v247, vcc, 0, v247, vcc
	v_cmp_le_i32_e32 vcc, v250, v0
	s_nop 1
	v_addc_co_u32_e32 v247, vcc, 0, v247, vcc
	v_cmp_le_i32_e32 vcc, v251, v0
	s_nop 1
	v_addc_co_u32_e32 v247, vcc, 0, v247, vcc
	ds_read_b128 v[248:251], v1 offset:64
	s_waitcnt lgkmcnt(0)
	v_cmp_le_i32_e32 vcc, v248, v0
	s_nop 1
	v_addc_co_u32_e32 v247, vcc, 0, v247, vcc
	v_cmp_le_i32_e32 vcc, v249, v0
	s_nop 1
	v_addc_co_u32_e32 v247, vcc, 0, v247, vcc
	v_cmp_le_i32_e32 vcc, v250, v0
	s_nop 1
	v_addc_co_u32_e32 v247, vcc, 0, v247, vcc
	v_cmp_le_i32_e32 vcc, v251, v0
	s_nop 1
	v_addc_co_u32_e32 v247, vcc, 0, v247, vcc
	ds_read_b128 v[248:251], v1 offset:80
	s_waitcnt lgkmcnt(0)
	v_cmp_le_i32_e32 vcc, v248, v0
	s_nop 1
	v_addc_co_u32_e32 v247, vcc, 0, v247, vcc
	v_cmp_le_i32_e32 vcc, v249, v0
	s_nop 1
	v_addc_co_u32_e32 v247, vcc, 0, v247, vcc
	v_cmp_le_i32_e32 vcc, v250, v0
	s_nop 1
	v_addc_co_u32_e32 v247, vcc, 0, v247, vcc
	v_cmp_le_i32_e32 vcc, v251, v0
	s_nop 1
	v_addc_co_u32_e32 v247, vcc, 0, v247, vcc
	ds_read_b128 v[248:251], v1 offset:96
	s_waitcnt lgkmcnt(0)
	v_cmp_le_i32_e32 vcc, v248, v0
	s_nop 1
	v_addc_co_u32_e32 v247, vcc, 0, v247, vcc
	v_cmp_le_i32_e32 vcc, v249, v0
	s_nop 1
	v_addc_co_u32_e32 v247, vcc, 0, v247, vcc
	v_cmp_le_i32_e32 vcc, v250, v0
	s_nop 1
	v_addc_co_u32_e32 v247, vcc, 0, v247, vcc
	v_cmp_le_i32_e32 vcc, v251, v0
	s_nop 1
	v_addc_co_u32_e32 v247, vcc, 0, v247, vcc
	ds_read_b128 v[248:251], v1 offset:112
	s_waitcnt lgkmcnt(0)
	v_cmp_le_i32_e32 vcc, v248, v0
	s_nop 1
	v_addc_co_u32_e32 v247, vcc, 0, v247, vcc
	v_cmp_le_i32_e32 vcc, v249, v0
	s_nop 1
	v_addc_co_u32_e32 v247, vcc, 0, v247, vcc
	v_cmp_le_i32_e32 vcc, v250, v0
	s_nop 1
	v_addc_co_u32_e32 v247, vcc, 0, v247, vcc
	v_cmp_le_i32_e32 vcc, v251, v0
	s_nop 1
	v_addc_co_u32_e32 v247, vcc, 0, v247, vcc
	ds_read_b32 v248, v1 offset:128
	s_waitcnt lgkmcnt(0)
	v_cmp_lt_i32_e32 vcc, v0, v248
	s_and_saveexec_b64 s[2:3], vcc
	v_lshlrev_b32_e32 v249, 2, v0
	v_add_u32_e32 v249, 0x21200, v249
	ds_write_b32 v249, v247
	s_or_b64 exec, exec, s[2:3]
	s_add_i32 s2, 0, 0x20480
	v_mov_b32_e32 v1, s2
	v_readlane_b32 s2, v246, 12
	s_waitcnt lgkmcnt(0)
	s_barrier
	ds_read_b32 v1, v1
	s_and_b32 s12, s2, 7
	s_lshl_b32 s2, s12, 8
	s_add_u32 s2, s92, s2
	s_addc_u32 s3, s93, 0
	s_add_u32 s2, s2, 0x10800
	s_waitcnt lgkmcnt(0)
	v_readfirstlane_b32 s33, v1
	s_addc_u32 s3, s3, 0
	s_and_saveexec_b64 s[4:5], s[0:1]
	s_cbranch_execz .LBB0_1441
	s_mov_b64 s[8:9], exec
	v_mbcnt_lo_u32_b32 v1, s8, 0
	v_mbcnt_hi_u32_b32 v1, s9, v1
	v_cmp_eq_u32_e32 vcc, 0, v1
	s_and_saveexec_b64 s[6:7], vcc
	s_cbranch_execz .LBB0_1438
	s_bcnt1_i32_b64 s8, s[8:9]
	v_mov_b32_e32 v2, 0
	v_mov_b32_e32 v3, s8
	global_atomic_add v2, v2, v3, s[2:3] sc0
